# speedup vs baseline: 1.0465x; 1.0032x over previous
.LBB2_12:
	ds_bpermute_b32 v35, v138, v34
	v_lshlrev_b32_e32 v116, 12, v132
	v_or_b32_e32 v39, v116, v130
	v_mov_b32_e32 v119, v117
	v_mov_b32_e32 v131, 0
	v_lshlrev_b64 v[142:143], 12, v[118:119]
	s_mov_b64 s[56:57], 0x4000
	v_lshl_add_u64 v[142:143], s[44:45], 0, v[142:143]
	v_lshl_add_u64 v[144:145], v[114:115], 0, s[56:57]
	v_lshl_add_u64 v[142:143], v[142:143], 0, v[130:131]
	global_load_dwordx4 v[50:53], v[142:143], off
	global_load_dwordx4 v[54:57], v[142:143], off offset:1024
	global_load_dwordx4 v[58:61], v[142:143], off offset:2048
	global_load_dwordx4 v[62:65], v[142:143], off offset:3072
	global_load_dwordx4 v[98:101], v[144:145], off offset:3072
	global_load_dwordx4 v[102:105], v[144:145], off offset:2048
	global_load_dwordx4 v[106:109], v[144:145], off offset:1024
	s_waitcnt lgkmcnt(0)
	v_add_f32_e32 v34, v34, v35
	v_div_scale_f32 v35, s[2:3], v34, v34, 1.0
	v_rcp_f32_e32 v36, v35
	v_div_scale_f32 v37, vcc, 1.0, v34, 1.0
	s_movk_i32 s2, 0x4000
	v_fma_f32 v38, -v35, v36, 1.0
	v_fmac_f32_e32 v36, v38, v36
	v_mul_f32_e32 v38, v37, v36
	v_fma_f32 v40, -v35, v38, v37
	v_fmac_f32_e32 v38, v40, v36
	v_fma_f32 v35, -v35, v38, v37
	v_div_fmas_f32 v35, v35, v36, v38
	v_div_fixup_f32 v38, v35, v34, 1.0
	v_fma_mixlo_f16 v34, v38, v18, 0
	v_mov_b32_e32 v18, v19
	v_mov_b32_e32 v19, v20
	v_mov_b32_e32 v20, v21
	v_mov_b32_e32 v21, v22
	v_pk_mul_f32 v[20:21], v[38:39], v[20:21] op_sel_hi:[0,1]
	v_cvt_pk_f16_f32 v22, v20, v21
	v_mov_b32_e32 v20, v23
	v_mov_b32_e32 v21, v24
	v_pk_mul_f32 v[20:21], v[38:39], v[20:21] op_sel_hi:[0,1]
	v_pk_mul_f32 v[18:19], v[38:39], v[18:19] op_sel_hi:[0,1]
	v_cvt_pk_f16_f32 v21, v20, v21
	v_cvt_pk_f16_f32 v19, v18, v19
	v_alignbit_b32 v20, v21, v22, 16
	v_lshrrev_b32_e32 v21, 16, v21
	v_pack_b32_f16 v18, v34, v19
	v_alignbit_b32 v19, v22, v19, 16
	v_fma_mixhi_f16 v21, v38, v25, 0
	ds_write_b128 v39, v[18:21]
	v_mov_b32_e32 v18, v27
	v_mov_b32_e32 v19, v28
	v_pk_mul_f32 v[18:19], v[38:39], v[18:19] op_sel_hi:[0,1]
	v_fma_mixlo_f16 v20, v38, v26, 0
	v_cvt_pk_f16_f32 v19, v18, v19
	v_pack_b32_f16 v18, v20, v19
	v_mov_b32_e32 v20, v29
	v_mov_b32_e32 v21, v30
	v_pk_mul_f32 v[20:21], v[38:39], v[20:21] op_sel_hi:[0,1]
	v_cvt_pk_f16_f32 v22, v20, v21
	v_mov_b32_e32 v20, v31
	v_mov_b32_e32 v21, v32
	v_pk_mul_f32 v[20:21], v[38:39], v[20:21] op_sel_hi:[0,1]
	v_cvt_pk_f16_f32 v21, v20, v21
	v_alignbit_b32 v20, v21, v22, 16
	v_lshrrev_b32_e32 v21, 16, v21
	v_alignbit_b32 v19, v22, v19, 16
	v_fma_mixhi_f16 v21, v38, v33, 0
	ds_write_b128 v39, v[18:21] offset:1024
	v_lshlrev_b64 v[18:19], 12, v[118:119]
	v_lshl_add_u64 v[18:19], s[44:45], 0, v[18:19]
	v_add_co_u32_e32 v20, vcc, s2, v114
	v_lshl_add_u64 v[18:19], v[18:19], 0, v[130:131]
	s_nop 0
	v_addc_co_u32_e32 v21, vcc, 0, v115, vcc
	global_load_dwordx4 v[34:37], v[20:21], off
	v_fma_mixlo_f16 v22, v38, v2, 0
	v_mov_b32_e32 v2, v3
	v_mov_b32_e32 v3, v4
	v_mov_b32_e32 v4, v5
	v_mov_b32_e32 v5, v6
	v_pk_mul_f32 v[4:5], v[38:39], v[4:5] op_sel_hi:[0,1]
	v_cvt_pk_f16_f32 v6, v4, v5
	v_mov_b32_e32 v4, v7
	v_mov_b32_e32 v5, v8
	v_pk_mul_f32 v[4:5], v[38:39], v[4:5] op_sel_hi:[0,1]
	v_pk_mul_f32 v[2:3], v[38:39], v[2:3] op_sel_hi:[0,1]
	v_cvt_pk_f16_f32 v5, v4, v5
	v_cvt_pk_f16_f32 v3, v2, v3
	v_alignbit_b32 v4, v5, v6, 16
	v_lshrrev_b32_e32 v5, 16, v5
	v_pack_b32_f16 v2, v22, v3
	v_alignbit_b32 v3, v6, v3, 16
	v_fma_mixhi_f16 v5, v38, v9, 0
	ds_write_b128 v39, v[2:5] offset:2048
	v_mov_b32_e32 v2, v11
	v_mov_b32_e32 v3, v12
	v_pk_mul_f32 v[2:3], v[38:39], v[2:3] op_sel_hi:[0,1]
	v_fma_mixlo_f16 v4, v38, v10, 0
	v_cvt_pk_f16_f32 v3, v2, v3
	v_pack_b32_f16 v2, v4, v3
	v_mov_b32_e32 v4, v13
	v_mov_b32_e32 v5, v14
	v_pk_mul_f32 v[4:5], v[38:39], v[4:5] op_sel_hi:[0,1]
	v_cvt_pk_f16_f32 v6, v4, v5
	v_mov_b32_e32 v4, v15
	v_mov_b32_e32 v5, v16
	v_pk_mul_f32 v[4:5], v[38:39], v[4:5] op_sel_hi:[0,1]
	v_cvt_pk_f16_f32 v5, v4, v5
	v_alignbit_b32 v4, v5, v6, 16
	v_lshrrev_b32_e32 v5, 16, v5
	s_xor_b32 s44, s52, 7
	v_alignbit_b32 v3, v6, v3, 16
	v_fma_mixhi_f16 v5, v38, v17, 0
	s_lshl_b32 s2, s44, 12
	s_mov_b32 s46, 4
	ds_write_b128 v39, v[2:5] offset:3072
	s_or_b32 s45, s54, 0xffffc000
	s_add_u32 s47, s2, 0xffffc000
	v_mov_b32_e32 v114, 0xff800000
	s_mov_b64 s[2:3], 0
	v_mov_b32_e32 v115, 0xff800000
	v_mov_b32_e32 v2, v131
	v_mov_b32_e32 v3, v131
	v_mov_b32_e32 v4, v131
	v_mov_b32_e32 v5, v131
	v_mov_b32_e32 v6, v131
	v_mov_b32_e32 v7, v131
	v_mov_b32_e32 v8, v131
	v_mov_b32_e32 v9, v131
	v_mov_b32_e32 v10, v131
	v_mov_b32_e32 v11, v131
	v_mov_b32_e32 v12, v131
	v_mov_b32_e32 v13, v131
	v_mov_b32_e32 v14, v131
	v_mov_b32_e32 v15, v131
	v_mov_b32_e32 v16, v131
	v_mov_b32_e32 v17, v131
	v_mov_b32_e32 v18, v131
	v_mov_b32_e32 v19, v131
	v_mov_b32_e32 v20, v131
	v_mov_b32_e32 v21, v131
	v_mov_b32_e32 v22, v131
	v_mov_b32_e32 v23, v131
	v_mov_b32_e32 v24, v131
	v_mov_b32_e32 v25, v131
	v_mov_b32_e32 v26, v131
	v_mov_b32_e32 v27, v131
	v_mov_b32_e32 v28, v131
	v_mov_b32_e32 v29, v131
	s_waitcnt vmcnt(3)
	v_mov_b64_e32 v[66:67], v[98:99]
	s_waitcnt vmcnt(2)
	v_mov_b64_e32 v[70:71], v[102:103]
	s_waitcnt vmcnt(1)
	v_mov_b64_e32 v[74:75], v[106:107]
	s_waitcnt vmcnt(0)
	v_mov_b64_e32 v[80:81], v[36:37]
	v_mov_b32_e32 v30, v131
	v_mov_b32_e32 v31, v131
	v_mov_b32_e32 v32, v131
	v_mov_b32_e32 v33, v131
	v_mov_b64_e32 v[68:69], v[100:101]
	v_mov_b64_e32 v[72:73], v[104:105]
	v_mov_b64_e32 v[76:77], v[108:109]
	v_mov_b64_e32 v[78:79], v[34:35]

.LBB2_15:
	s_setprio 1
	v_mfma_f32_32x32x16_f16 v[34:49], v[34:37], v[50:53], 0
	v_mfma_f32_32x32x16_f16 v[34:49], v[106:109], v[54:57], v[34:49]
	v_mfma_f32_32x32x16_f16 v[34:49], v[102:105], v[58:61], v[34:49]
	v_mfma_f32_32x32x16_f16 v[34:49], v[98:101], v[62:65], v[34:49]
	s_setprio 0
	s_cmp_lg_u32 s47, s2
	s_cbranch_scc1 .LBB2_17
	s_nop 8
	v_cndmask_b32_e64 v98, v34, v114, s[4:5]
	v_cndmask_b32_e64 v35, v114, v35, s[6:7]
	v_cndmask_b32_e64 v34, v98, v34, s[6:7]
	v_cndmask_b32_e64 v36, v36, v114, s[8:9]
	v_cndmask_b32_e64 v37, v37, v114, s[10:11]
	v_cndmask_b32_e64 v38, v38, v114, s[12:13]
	v_cndmask_b32_e64 v39, v39, v114, s[14:15]
	v_cndmask_b32_e64 v40, v40, v114, s[16:17]
	v_cndmask_b32_e64 v41, v41, v114, s[18:19]
	v_cndmask_b32_e64 v42, v42, v114, s[20:21]
	v_cndmask_b32_e64 v43, v43, v114, s[22:23]
	v_cndmask_b32_e64 v44, v44, v114, s[24:25]
	v_cndmask_b32_e64 v45, v45, v114, s[26:27]
	v_cndmask_b32_e64 v46, v46, v114, s[28:29]
	v_cndmask_b32_e64 v47, v47, v114, s[30:31]
	v_cndmask_b32_e64 v48, v48, v114, s[34:35]
	v_cndmask_b32_e64 v49, v49, v114, s[36:37]
